# v7 + attention loops: hipcc's vmcnt(0) before the per-tile barrier removed (counted wait leaves the next tile's DMA in flight, two tiles ahead as designed)
# baseline (speedup 1.0000x reference)
; #define LAS __attribute__((address_space(3)))
; __device__ __forceinline__ int v_rd_base(int lane) { return ((lane & 3) << 3) | (((lane >> 2) & 3) << 6) | (((lane >> 4) & 1) << 5) | (((lane >> 5) & 1) << 8); }
; #define DMA_WAIT(last) do { if (last) asm volatile("s_waitcnt vmcnt(0)" ::: "memory"); else asm volatile("s_waitcnt vmcnt(%0)" :: "n"(NPW) : "memory"); } while (0)
; template <int DK>
; __device__ __forceinline__ void qkt(f32x16& p0, f32x16& p1, const char* Ks, const bf16x8* qr, int r32, int hi) {
;   p0 = f32x16{}; p1 = f32x16{};
; #pragma unroll
;   for (int d0 = 0; d0 < DK / 16; ++d0) { const int cb = (d0 * 16 + hi * 8) * 2;
;     const bf16x8 b0 = *reinterpret_cast<const bf16x8*>(Ks + ATT_KSWZ(r32, cb));
;     const bf16x8 b1 = *reinterpret_cast<const bf16x8*>(Ks + ATT_KSWZ(32 + r32, cb));
;     p0 = __builtin_amdgcn_mfma_f32_32x32x16_bf16(b0, qr[d0], p0, 0, 0, 0);
;     p1 = __builtin_amdgcn_mfma_f32_32x32x16_bf16(b1, qr[d0], p1, 0, 0, 0);
;   }
; }
; template <int DK, int DV, bool OFF, class QLoader> ...
;     ...
;   bf16x8 qr[DK / 16];
;   QL.load(qr, wid * QBLK + r32, hi);
;   asm volatile("s_waitcnt vmcnt(0)" ::: "memory");
;   unsigned koff[KPW], voff[VPW];
; #pragma unroll
;   for (int i = 0; i < (DK == 64 ? 1 : KPW); ++i) { const int row = (wid * KPW + i) * 4 + (lane >> 4); int c = (lane & 15) ^ (row & 7); c = (c < DK / 8) ? c : (c & 7); koff[i] = (unsigned)((row * ldk) * 2 + c * 16); }
; #pragma unroll
;   for (int i = 0; i < 1; ++i) { const int sidx = (wid * VPW + i) * 2 + (lane >> 5), kg = sidx / ND, st = sidx % ND, kk = kg * 8 + ((lane & 31) >> 2);
;     const int k = (kk & ~0xC) | ((kk & 4) << 1) | ((kk & 8) >> 1), c = st * 32 + (lane & 3) * 8; voff[i] = (unsigned)((k * ldv + c) * 2); }
;   const int vb0 = (int)(uintptr_t)V_lds + v_rd_base(lane);
;   LAS unsigned* const ldsK = (LAS unsigned*)(LAS char*)K_lds + (wid * KPW) * 256; LAS unsigned* const ldsV = (LAS unsigned*)(LAS char*)V_lds + (wid * VPW) * 256;
;     ...
;   f32x16 pA0, pA1, pB0, pB1; bf16x8 pa0, pa1, pa2, pa3; const int NT = nkeys / KVBLK;
;   DMA_TILE(0, 0); DMA_TILE(1, 1); DMA_WAIT(false); __syncthreads(); if (2 < NT) DMA_TILE(2, 2);
;   qkt<DK>(pA0, pA1, K_lds, qr, r32, hi); partialSM<DK, OFF>(pA0, pA1, negMC);
.LBB0_838:
	s_and_b64 s[16:17], s[14:15], exec
	s_cselect_b32 s76, s12, s2
	s_ashr_i32 s2, s76, 4
	s_and_b32 s22, s76, 15
	s_mul_i32 s78, s76, 0x88000
	s_mul_hi_i32 s77, s76, 0x88000
	s_add_u32 s16, s65, s78
	s_addc_u32 s17, s66, s77
	s_lshl_b32 s4, s2, 8
	s_add_i32 s23, s4, 0x8000
	s_mul_i32 s80, s23, 0x1800
	s_mul_hi_i32 s79, s23, 0x1800
	s_add_u32 s4, s67, s80
	s_addc_u32 s12, s68, s79
	s_lshl_b32 s13, s76, 7
	s_and_b32 s13, s13, 0x700
	s_add_u32 s4, s4, s13
	s_addc_u32 s12, s12, 0
	s_add_u32 s18, s4, 0x1000
	s_addc_u32 s19, s12, 0
	s_lshl_b32 s12, s2, 12
	s_mul_i32 s2, s2, 0x1800000
	s_mul_hi_i32 s4, s12, 0x1800
	s_add_u32 s24, s67, s2
	s_addc_u32 s25, s68, s4
	s_add_u32 s13, s24, s13
	s_addc_u32 s24, s25, 0
	s_add_u32 s74, s13, 0x1000
	s_addc_u32 s75, s24, 0
	s_lshl_b32 s5, s5, 8
	s_or_b32 s5, s12, s5
	s_and_b64 s[12:13], s[14:15], exec
	s_cselect_b32 s12, s5, s23
	s_ashr_i32 s13, s12, 31
	s_lshl_b64 s[12:13], s[12:13], 12
	s_add_u32 s5, s69, s12
	s_addc_u32 s13, s70, s13
	s_lshl_b32 s12, s22, 8
	s_add_u32 s12, s5, s12
	s_addc_u32 s13, s13, 0
	s_andn2_b64 vcc, exec, s[34:35]
	s_mov_b64 s[22:23], -1
	s_cbranch_vccnz .LBB0_882
	v_mov_b32_e32 v25, v159
	v_mov_b32_e32 v33, v1
	v_readfirstlane_b32 s23, v25
	s_ashr_i32 s26, s23, 6
	v_and_b32_e32 v10, 31, v25
	s_lshl_b32 s22, s26, 5
	v_or_b32_e32 v2, s22, v10
	v_ashrrev_i32_e32 v3, 31, v2
	v_bfe_u32 v4, v25, 5, 1
	v_lshlrev_b64 v[2:3], 7, v[2:3]
	v_lshl_add_u64 v[2:3], s[20:21], 0, v[2:3]
	v_lshlrev_b32_e32 v32, 4, v4
	v_lshl_add_u64 v[2:3], v[2:3], 0, v[32:33]
	global_load_dwordx4 v[114:117], v[2:3], off
	global_load_dwordx4 v[118:121], v[2:3], off offset:32
	global_load_dwordx4 v[122:125], v[2:3], off offset:64
	global_load_dwordx4 v[126:129], v[2:3], off offset:96
	v_bfe_u32 v0, v25, 4, 2
	s_bfe_i32 s24, s26, 0x1001d
	v_and_b32_e32 v2, 15, v25
	v_bitop3_b32 v3, v0, v25, 15 bitop3:0x78
	v_lshl_or_b32 v20, s26, 2, v4
	s_lshr_b32 s24, s24, 30
	v_lshlrev_b32_e32 v3, 4, v3
	v_cmp_gt_u32_e32 vcc, 8, v2
	v_add_u32_e32 v2, s24, v20
	v_and_b32_e32 v5, 0x70, v3
	v_ashrrev_i32_e32 v21, 2, v2
	v_cndmask_b32_e32 v19, v5, v3, vcc
	v_lshlrev_b32_e32 v4, 3, v21
	v_bfe_u32 v5, v25, 2, 3
	v_bitop3_b32 v22, v4, -13, v5 bitop3:0xc8
	v_lshrrev_b32_e32 v4, 1, v25
	s_lshl_b32 s5, s26, 10
	v_lshlrev_b32_e32 v18, 7, v0
	v_and_b32_e32 v23, 8, v4
	v_and_b32_e32 v26, 4, v2
	v_or_b32_e32 v0, s5, v18
	v_and_b32_e32 v3, 0x3fffffc, v2
	v_or3_b32 v2, v23, v22, v26
	s_movk_i32 s24, 0xc00
	v_add_u32_e32 v0, v0, v19
	v_lshlrev_b32_e32 v4, 3, v25
	v_mul_lo_u32 v2, v2, s24
	s_add_i32 s27, 0, 0x10000
	s_lshl_b32 s24, s26, 11
	v_sub_u32_e32 v3, v20, v3
	v_and_b32_e32 v24, 24, v4
	s_add_i32 s81, s27, s24
	v_xor_b32_e32 v150, 64, v0
	v_mov_b32_e32 v151, v1
	v_lshl_or_b32 v3, v3, 5, v24
	s_add_i32 s82, s24, 0
	s_mov_b32 m0, s81
	v_lshl_add_u64 v[4:5], s[16:17], 0, v[150:151]
	s_mov_b64 s[24:25], 0x200
	s_add_i32 s83, s81, 0x400
	v_add_lshl_u32 v148, v3, v2, 1
	global_load_lds_dwordx4 v0, s[16:17]
	v_lshl_add_u64 v[6:7], v[4:5], 0, s[24:25]
	s_mov_b32 m0, s83
	v_mov_b32_e32 v149, v1
	global_load_lds_dwordx4 v[6:7], off
	v_lshl_add_u64 v[6:7], s[18:19], 0, v[148:149]
	s_mov_b32 m0, s82
	s_add_i32 s84, s82, 0x400
	v_lshl_add_u64 v[2:3], s[16:17], 0, v[0:1]
	global_load_lds_dwordx4 v148, s[18:19]
	v_lshl_add_u64 v[8:9], v[6:7], 0, s[10:11]
	s_mov_b32 m0, s84
	s_mov_b64 s[24:25], 0x2000
	s_add_i32 s85, s81, 0x4000
	global_load_lds_dwordx4 v[8:9], off
	v_lshl_add_u64 v[8:9], v[2:3], 0, s[24:25]
	s_mov_b32 m0, s85
	s_mov_b64 s[24:25], 0x2200
	s_add_i32 s86, s81, 0x4400
	global_load_lds_dwordx4 v[8:9], off
	v_lshl_add_u64 v[8:9], v[4:5], 0, s[24:25]
	s_mov_b32 m0, s86
	s_mov_b64 s[24:25], 0x60000
	s_add_i32 s87, s82, 0x4000
	global_load_lds_dwordx4 v[8:9], off
	v_lshl_add_u64 v[8:9], v[6:7], 0, s[24:25]
	s_mov_b32 m0, s87
	s_mov_b64 s[24:25], 0x60080
	s_add_i32 s88, s82, 0x4400
	global_load_lds_dwordx4 v[8:9], off
	v_lshl_add_u64 v[8:9], v[6:7], 0, s[24:25]
	s_mov_b32 m0, s88
	s_mov_b64 s[24:25], 0x4000
	s_add_i32 s89, s81, 0x8000
	global_load_lds_dwordx4 v[8:9], off
	v_lshl_add_u64 v[2:3], v[2:3], 0, s[24:25]
	s_mov_b32 m0, s89
	s_mov_b64 s[24:25], 0x4200
	s_add_i32 s90, s81, 0x8400
	s_waitcnt vmcnt(4)
	s_waitcnt lgkmcnt(0)
	s_barrier
	global_load_lds_dwordx4 v[2:3], off
	v_lshl_add_u64 v[2:3], v[4:5], 0, s[24:25]
	s_mov_b32 m0, s90
	s_mov_b64 s[24:25], 0xc0000
	s_add_i32 s91, s82, 0x8000
	global_load_lds_dwordx4 v[2:3], off
	v_lshl_add_u64 v[2:3], v[6:7], 0, s[24:25]
	s_mov_b32 m0, s91
	s_mov_b64 s[24:25], 0xc0080
	s_add_i32 s92, s82, 0x8400
	global_load_lds_dwordx4 v[2:3], off
	v_lshl_add_u64 v[2:3], v[6:7], 0, s[24:25]
	s_mov_b32 m0, s92
	v_lshlrev_b32_e32 v27, 8, v10
	global_load_lds_dwordx4 v[2:3], off
	v_lshlrev_b32_e32 v2, 4, v25
	v_and_b32_e32 v33, 0x70, v2
	v_bitop3_b32 v161, v32, v27, v33 bitop3:0xde
	v_add_u32_e32 v162, s27, v161
	ds_read_b128 v[2:5], v162
	ds_read_b128 v[28:31], v162 offset:8192
	s_waitcnt lgkmcnt(0)
	v_mfma_f32_32x32x16_bf16 v[66:81], v[28:31], v[114:117], 0
	v_or_b32_e32 v28, 32, v32
	v_bitop3_b32 v163, v28, v27, v33 bitop3:0xde
	v_add_u32_e32 v164, s27, v163
	ds_read_b128 v[28:31], v164
	s_cmp_lt_i32 s26, 4
	v_mfma_f32_32x32x16_bf16 v[2:17], v[2:5], v[114:117], 0
	s_waitcnt lgkmcnt(0)
	v_mfma_f32_32x32x16_bf16 v[2:17], v[28:31], v[118:121], v[2:17]
	ds_read_b128 v[28:31], v164 offset:8192
	s_waitcnt lgkmcnt(0)
	v_mfma_f32_32x32x16_bf16 v[66:81], v[28:31], v[118:121], v[66:81]
	v_or_b32_e32 v28, 64, v32
	v_bitop3_b32 v165, v28, v27, v33 bitop3:0xde
	v_add_u32_e32 v166, s27, v165
	ds_read_b128 v[28:31], v166
	s_waitcnt lgkmcnt(0)
	v_mfma_f32_32x32x16_bf16 v[2:17], v[28:31], v[122:125], v[2:17]
	ds_read_b128 v[28:31], v166 offset:8192
	s_waitcnt lgkmcnt(0)
	v_mfma_f32_32x32x16_bf16 v[66:81], v[28:31], v[122:125], v[66:81]
	v_or_b32_e32 v28, 0x60, v32
	v_bitop3_b32 v167, v28, v27, v33 bitop3:0xde
	v_add_u32_e32 v168, s27, v167
	ds_read_b128 v[28:31], v168
	s_waitcnt lgkmcnt(0)
	v_mfma_f32_32x32x16_bf16 v[2:17], v[28:31], v[126:129], v[2:17]
	ds_read_b128 v[28:31], v168 offset:8192
	s_waitcnt lgkmcnt(0)
	v_mfma_f32_32x32x16_bf16 v[66:81], v[28:31], v[126:129], v[66:81]
	s_cbranch_scc1 .LBB0_841
	s_setprio 1

; #define DMA_WAIT(last) do { if (last) asm volatile("s_waitcnt vmcnt(0)" ::: "memory"); else asm volatile("s_waitcnt vmcnt(%0)" :: "n"(NPW) : "memory"); } while (0)
; template <int DK, int DV, bool OFF, class QLoader> ...
;     ...
;   f32x16 pA0, pA1, pB0, pB1; bf16x8 pa0, pa1, pa2, pa3; const int NT = nkeys / KVBLK;
;   DMA_TILE(0, 0); DMA_TILE(1, 1); DMA_WAIT(false); __syncthreads(); if (2 < NT) DMA_TILE(2, 2);
;   qkt<DK>(pA0, pA1, K_lds, qr, r32, hi); partialSM<DK, OFF>(pA0, pA1, negMC);
.LBB0_846:
	s_add_i32 s28, s55, -3
	s_cmp_lt_u32 s28, s95
	s_cselect_b64 s[24:25], -1, 0
	s_cmp_ge_u32 s28, s95
	s_cselect_b64 s[28:29], -1, 0
	s_and_b64 vcc, exec, s[28:29]
	s_barrier
	s_cbranch_vccnz .LBB0_856
	s_cmp_gt_u32 s57, 1
	s_cselect_b64 s[36:37], -1, 0
	s_mov_b64 s[38:39], -1
	s_and_b64 vcc, exec, s[36:37]
	s_cbranch_vccz .LBB0_851
	s_lshl_b64 s[30:31], s[2:3], 7
	s_add_u32 s30, s93, s30
	s_addc_u32 s31, s94, s31
	s_cbranch_execz .LBB0_852

; #define DMA_WAIT(last) do { if (last) asm volatile("s_waitcnt vmcnt(0)" ::: "memory"); else asm volatile("s_waitcnt vmcnt(%0)" :: "n"(NPW) : "memory"); } while (0)
; template <int DK, int DV, bool OFF, class QLoader> ...
;     ...
;   f32x16 pA0, pA1, pB0, pB1; bf16x8 pa0, pa1, pa2, pa3; const int NT = nkeys / KVBLK;
;   DMA_TILE(0, 0); DMA_TILE(1, 1); DMA_WAIT(false); __syncthreads(); if (2 < NT) DMA_TILE(2, 2);
;   qkt<DK>(pA0, pA1, K_lds, qr, r32, hi); partialSM<DK, OFF>(pA0, pA1, negMC);
.LBB0_861:
	s_add_i32 s26, s55, -2
	s_cmp_ge_u32 s26, s95
	s_barrier
	s_cbranch_scc1 .LBB0_863
	v_lshl_add_u64 v[66:67], v[156:157], 0, s[8:9]
	s_mov_b64 s[26:27], 0x1ec08000
	s_mov_b32 m0, s81
	v_lshl_add_u64 v[66:67], v[66:67], 0, s[26:27]
	global_load_lds_dwordx4 v[66:67], off
	v_lshl_add_u64 v[66:67], v[154:155], 0, s[8:9]
	s_mov_b64 s[26:27], 0x1ec08200
	v_lshl_add_u64 v[66:67], v[66:67], 0, s[26:27]
	s_mov_b32 m0, s83
	s_mov_b64 s[26:27], 0xdc01000
	global_load_lds_dwordx4 v[66:67], off
	v_lshl_add_u64 v[66:67], v[152:153], 0, s[8:9]
	v_lshl_add_u64 v[68:69], v[66:67], 0, s[26:27]
	s_mov_b32 m0, s82
	s_mov_b64 s[26:27], 0xdc01080
	global_load_lds_dwordx4 v[68:69], off
	v_lshl_add_u64 v[66:67], v[66:67], 0, s[26:27]
	s_mov_b32 m0, s84
	s_nop 0
	global_load_lds_dwordx4 v[66:67], off

; #define DMA_WAIT(last) do { if (last) asm volatile("s_waitcnt vmcnt(0)" ::: "memory"); else asm volatile("s_waitcnt vmcnt(%0)" :: "n"(NPW) : "memory"); } while (0)
; template <int DK, int DV, bool OFF, class QLoader> ...
;     ...
;   f32x16 pA0, pA1, pB0, pB1; bf16x8 pa0, pa1, pa2, pa3; const int NT = nkeys / KVBLK;
;   DMA_TILE(0, 0); DMA_TILE(1, 1); DMA_WAIT(false); __syncthreads(); if (2 < NT) DMA_TILE(2, 2);
;   qkt<DK>(pA0, pA1, K_lds, qr, r32, hi); partialSM<DK, OFF>(pA0, pA1, negMC);
.LBB0_870:
	s_add_i32 s24, s55, -1
	s_cmp_ge_u32 s24, s95
	s_barrier
	s_cbranch_scc1 .LBB0_872
	v_lshl_add_u64 v[82:83], v[156:157], 0, s[8:9]
	s_mov_b64 s[24:25], 0x1ec0a000
	s_mov_b32 m0, s85
	v_lshl_add_u64 v[82:83], v[82:83], 0, s[24:25]
	global_load_lds_dwordx4 v[82:83], off
	v_lshl_add_u64 v[82:83], v[154:155], 0, s[8:9]
	s_mov_b64 s[24:25], 0x1ec0a200
	v_lshl_add_u64 v[82:83], v[82:83], 0, s[24:25]
	s_mov_b32 m0, s86
	s_mov_b64 s[24:25], 0xdc61000
	global_load_lds_dwordx4 v[82:83], off
	v_lshl_add_u64 v[82:83], v[152:153], 0, s[8:9]
	v_lshl_add_u64 v[84:85], v[82:83], 0, s[24:25]
	s_mov_b32 m0, s87
	s_mov_b64 s[24:25], 0xdc61080
	global_load_lds_dwordx4 v[84:85], off
	v_lshl_add_u64 v[82:83], v[82:83], 0, s[24:25]
	s_mov_b32 m0, s88
	s_nop 0
	global_load_lds_dwordx4 v[82:83], off

; #define DMA_WAIT(last) do { if (last) asm volatile("s_waitcnt vmcnt(0)" ::: "memory"); else asm volatile("s_waitcnt vmcnt(%0)" :: "n"(NPW) : "memory"); } while (0)
; template <int DK, int DV, bool OFF, class QLoader> ...
;     ...
;   f32x16 pA0, pA1, pB0, pB1; bf16x8 pa0, pa1, pa2, pa3; const int NT = nkeys / KVBLK;
;   DMA_TILE(0, 0); DMA_TILE(1, 1); DMA_WAIT(false); __syncthreads(); if (2 < NT) DMA_TILE(2, 2);
;   qkt<DK>(pA0, pA1, K_lds, qr, r32, hi); partialSM<DK, OFF>(pA0, pA1, negMC);
.LBB0_877:
	s_cmp_ge_u32 s55, s95
	s_barrier
	s_cbranch_scc1 .LBB0_879
	v_lshl_add_u64 v[66:67], v[156:157], 0, s[8:9]
	s_mov_b64 s[24:25], 0x1ec0c000
	s_mov_b32 m0, s89
	v_lshl_add_u64 v[66:67], v[66:67], 0, s[24:25]
	global_load_lds_dwordx4 v[66:67], off
	v_lshl_add_u64 v[66:67], v[154:155], 0, s[8:9]
	s_mov_b64 s[24:25], 0x1ec0c200
	v_lshl_add_u64 v[66:67], v[66:67], 0, s[24:25]
	s_mov_b32 m0, s90
	s_mov_b64 s[24:25], 0xdcc1000
	global_load_lds_dwordx4 v[66:67], off
	v_lshl_add_u64 v[66:67], v[152:153], 0, s[8:9]
	v_lshl_add_u64 v[68:69], v[66:67], 0, s[24:25]
	s_mov_b32 m0, s91
	s_mov_b64 s[24:25], 0xdcc1080
	global_load_lds_dwordx4 v[68:69], off
	v_lshl_add_u64 v[66:67], v[66:67], 0, s[24:25]
	s_mov_b32 m0, s92
	s_nop 0
	global_load_lds_dwordx4 v[66:67], off

; #define LAS __attribute__((address_space(3)))
; __device__ __forceinline__ int v_rd_base(int lane) { return ((lane & 3) << 3) | (((lane >> 2) & 3) << 6) | (((lane >> 4) & 1) << 5) | (((lane >> 5) & 1) << 8); }
; __device__ __forceinline__ bf16x8 pack_bf8(const float* f) { u32x4 w = {cvtpk(f[0], f[1]), cvtpk(f[2], f[3]), cvtpk(f[4], f[5]), cvtpk(f[6], f[7])}; return *reinterpret_cast<bf16x8*>(&w); }
;   __device__ __forceinline__ void load(bf16x8 (&qr)[6], int r, int hi) const {
;     ...
; #pragma unroll
;     for (int d0 = 0; d0 < 6; ++d0) { const f32x4 g0 = *(const f32x4*)(gq + d0 * 16 + hi * 8), g1 = *(const f32x4*)(gq + d0 * 16 + hi * 8 + 4);
; #pragma unroll
;       for (int j = 0; j < 4; ++j) { v[d0][j] *= f * g0[j]; v[d0][4 + j] *= f * g1[j]; } }
;     if (cosA) { const float* c = cosA + (long)r * 16 + hi * 8; const float* sn = c + 4096 * 16;
; #pragma unroll
;       for (int j = 0; j < 8; ++j) { const float x1 = v[4][j], x2 = v[5][j], cs = c[j], si = sn[j]; v[4][j] = x1 * cs - x2 * si; v[5][j] = x1 * si + x2 * cs; } }
; #pragma unroll
;     for (int d0 = 0; d0 < 6; ++d0) qr[d0] = pack_bf8(v[d0]);
; template <int DK, int DV, bool OFF, class QLoader> ...
;     ...
;   unsigned koff[KPW], voff[VPW];
; #pragma unroll
;   for (int i = 0; i < (DK == 64 ? 1 : KPW); ++i) { const int row = (wid * KPW + i) * 4 + (lane >> 4); int c = (lane & 15) ^ (row & 7); c = (c < DK / 8) ? c : (c & 7); koff[i] = (unsigned)((row * ldk) * 2 + c * 16); }
; #pragma unroll
;   for (int i = 0; i < 1; ++i) { const int sidx = (wid * VPW + i) * 2 + (lane >> 5), kg = sidx / ND, st = sidx % ND, kk = kg * 8 + ((lane & 31) >> 2);
;     const int k = (kk & ~0xC) | ((kk & 4) << 1) | ((kk & 8) >> 1), c = st * 32 + (lane & 3) * 8; voff[i] = (unsigned)((k * ldv + c) * 2); }
;   const int vb0 = (int)(uintptr_t)V_lds + v_rd_base(lane);
;   LAS unsigned* const ldsK = (LAS unsigned*)(LAS char*)K_lds + (wid * KPW) * 256; LAS unsigned* const ldsV = (LAS unsigned*)(LAS char*)V_lds + (wid * VPW) * 256;
;     ...
;   f32x16 pA0, pA1, pB0, pB1; bf16x8 pa0, pa1, pa2, pa3; const int NT = nkeys / KVBLK;
;   DMA_TILE(0, 0); DMA_TILE(1, 1); DMA_WAIT(false); __syncthreads(); if (2 < NT) DMA_TILE(2, 2);
;   qkt<DK>(pA0, pA1, K_lds, qr, r32, hi); partialSM<DK, OFF>(pA0, pA1, negMC);
.LBB0_1415:
	v_and_b32_e32 v36, 63, v56
	v_mul_f32_e32 v0, v54, v33
	v_mul_f32_e32 v3, v3, v54
	v_mul_f32_e32 v0, v0, v88
	v_mul_f32_e32 v29, v54, v29
	v_mul_f32_e32 v32, v54, v32
	v_mul_f32_e32 v28, v54, v28
	v_mul_f32_e32 v31, v54, v31
	v_mul_f32_e32 v27, v54, v27
	v_mul_f32_e32 v30, v54, v30
	v_mul_f32_e32 v26, v54, v26
	v_mul_f32_e32 v25, v54, v25
	v_mul_f32_e32 v21, v21, v54
	v_mul_f32_e32 v24, v54, v24
	v_mul_f32_e32 v20, v20, v54
	v_mul_f32_e32 v23, v54, v23
	v_mul_f32_e32 v19, v19, v54
	v_mul_f32_e32 v22, v54, v22
	v_mul_f32_e32 v18, v18, v54
	v_mul_f32_e32 v17, v17, v54
	v_mul_f32_e32 v13, v13, v54
	v_mul_f32_e32 v16, v16, v54
	v_mul_f32_e32 v12, v12, v54
	v_mul_f32_e32 v15, v15, v54
	v_mul_f32_e32 v11, v11, v54
	v_mul_f32_e32 v14, v14, v54
	v_mul_f32_e32 v10, v10, v54
	v_mul_f32_e32 v9, v9, v54
	v_mul_f32_e32 v5, v5, v54
	v_mul_f32_e32 v8, v8, v54
	v_mul_f32_e32 v4, v4, v54
	v_mul_f32_e32 v7, v7, v54
	v_mul_f32_e32 v3, v3, v58
	v_mul_f32_e32 v6, v6, v54
	v_mul_f32_e32 v2, v2, v54
	v_lshrrev_b32_e32 v149, 4, v36
	v_mul_f32_e32 v29, v29, v86
	v_mul_f32_e32 v32, v32, v87
	v_mul_f32_e32 v28, v28, v84
	v_mul_f32_e32 v31, v31, v85
	v_mul_f32_e32 v27, v27, v82
	v_mul_f32_e32 v30, v30, v83
	v_mul_f32_e32 v26, v26, v81
	v_mul_f32_e32 v25, v25, v80
	v_mul_f32_e32 v21, v21, v78
	v_mul_f32_e32 v24, v24, v79
	v_mul_f32_e32 v20, v20, v76
	v_mul_f32_e32 v23, v23, v77
	v_mul_f32_e32 v19, v19, v74
	v_mul_f32_e32 v22, v22, v75
	v_mul_f32_e32 v18, v18, v73
	v_mul_f32_e32 v17, v17, v72
	v_mul_f32_e32 v13, v13, v70
	v_mul_f32_e32 v16, v16, v71
	v_mul_f32_e32 v12, v12, v68
	v_mul_f32_e32 v15, v15, v69
	v_mul_f32_e32 v11, v11, v66
	v_mul_f32_e32 v14, v14, v67
	v_mul_f32_e32 v10, v10, v65
	v_mul_f32_e32 v9, v9, v64
	v_mul_f32_e32 v5, v5, v62
	v_mul_f32_e32 v8, v8, v63
	v_mul_f32_e32 v4, v4, v60
	v_mul_f32_e32 v7, v7, v61
	v_mul_f32_e32 v6, v6, v59
	v_mul_f32_e32 v2, v2, v35
	v_cvt_pk_bf16_f32 v98, v2, v3
	v_cvt_pk_bf16_f32 v99, v4, v5
	v_cvt_pk_bf16_f32 v100, v6, v7
	v_cvt_pk_bf16_f32 v101, v8, v9
	v_cvt_pk_bf16_f32 v102, v10, v11
	v_cvt_pk_bf16_f32 v103, v12, v13
	v_cvt_pk_bf16_f32 v104, v14, v15
	v_cvt_pk_bf16_f32 v105, v16, v17
	v_cvt_pk_bf16_f32 v106, v18, v19
	v_cvt_pk_bf16_f32 v107, v20, v21
	v_cvt_pk_bf16_f32 v108, v22, v23
	v_cvt_pk_bf16_f32 v109, v24, v25
	v_cvt_pk_bf16_f32 v110, v26, v27
	v_cvt_pk_bf16_f32 v111, v28, v29
	v_cvt_pk_bf16_f32 v112, v30, v31
	v_cvt_pk_bf16_f32 v113, v32, v0
	v_lshl_or_b32 v0, s38, 3, v149
	v_bitop3_b32 v3, v149, v56, 15 bitop3:0x78
	s_movk_i32 s0, 0xc0
	v_and_b32_e32 v2, 15, v56
	v_mul_lo_u32 v4, v0, s0
	v_lshlrev_b32_e32 v0, 4, v3
	v_and_b32_e32 v3, 0x70, v0
	v_cmp_gt_u32_e32 vcc, 12, v2
	v_bitop3_b32 v2, v149, v2, 4 bitop3:0x36
	v_lshl_or_b32 v153, s38, 1, v57
	v_cndmask_b32_e32 v151, v3, v0, vcc
	v_lshlrev_b32_e32 v3, 4, v2
	v_cmp_gt_u32_e32 vcc, 12, v2
	v_lshrrev_b32_e32 v2, 31, v153
	v_and_b32_e32 v5, 0x70, v3
	v_add_u32_e32 v2, v153, v2
	v_cndmask_b32_e32 v150, v5, v3, vcc
	s_movk_i32 s0, 0x300
	v_ashrrev_i32_e32 v152, 1, v2
	v_add_u32_e32 v0, v151, v4
	v_add3_u32 v122, v4, v150, s0
	v_lshlrev_b32_e32 v3, 3, v152
	v_lshrrev_b32_e32 v4, 2, v55
	s_mov_b32 s0, 0x1fffff3
	v_bitop3_b32 v154, v3, s0, v4 bitop3:0xc8
	s_lshl_b32 s0, s38, 11
	v_lshrrev_b32_e32 v3, 1, v55
	s_add_i32 s87, s0, 0
	v_and_b32_e32 v2, 0x3fffffe, v2
	v_and_b32_e32 v155, 8, v3
	v_lshlrev_b32_e32 v3, 2, v152
	v_lshlrev_b32_e32 v4, 4, v56
	s_add_i32 s81, s87, 0x8000
	s_lshl_b32 s1, s38, 10
	v_cvt_pk_bf16_f32 v114, v50, v51
	v_cvt_pk_bf16_f32 v115, v52, v53
	v_cvt_pk_bf16_f32 v116, v40, v41
	v_cvt_pk_bf16_f32 v117, v46, v47
	v_cvt_pk_bf16_f32 v118, v44, v45
	v_cvt_pk_bf16_f32 v119, v48, v49
	v_cvt_pk_bf16_f32 v120, v38, v39
	v_cvt_pk_bf16_f32 v121, v42, v43
	s_waitcnt vmcnt(0)
	v_sub_u32_e32 v2, v153, v2
	v_and_b32_e32 v156, 4, v3
	v_and_b32_e32 v157, 48, v4
	s_sub_i32 s0, 0, s1
	s_sub_i32 s1, s87, s1
	s_mov_b32 m0, s81
	s_add_i32 s82, s87, 0x8400
	v_or3_b32 v3, v155, v154, v156
	v_lshl_or_b32 v2, v2, 6, v157
	s_mov_b32 m0, s82
	s_add_u32 s40, s20, 0x3000
	v_lshl_add_u32 v2, v3, 7, v2
	s_mov_b32 m0, s1
	s_addc_u32 s41, s21, 0
	s_add_i32 s83, s87, 0xc000
	s_mov_b32 m0, s83
	s_add_i32 s84, s87, 0xc400
	v_mov_b32_e32 v3, v1
	s_mov_b32 m0, s84
	v_lshl_add_u64 v[124:125], s[22:23], 0, v[2:3]
	s_mov_b64 s[40:41], 0x2000
	s_add_i32 m0, s1, 0x2000
	v_lshl_add_u64 v[2:3], v[124:125], 0, s[40:41]
	s_add_u32 s40, s20, 0x6000
	s_addc_u32 s41, s21, 0
	s_add_i32 m0, s87, 0x10000
	s_waitcnt vmcnt(3)
	s_waitcnt lgkmcnt(0)
	s_barrier
	global_load_lds_dwordx4 v0, s[40:41]
	s_add_i32 m0, s87, 0x10400
	v_lshlrev_b32_e32 v35, 8, v55
	global_load_lds_dwordx4 v122, s[40:41]
	s_mov_b64 s[40:41], 0x4000
	v_lshl_add_u64 v[2:3], v[124:125], 0, s[40:41]
	s_add_i32 m0, s1, 0x4000
	v_or_b32_e32 v38, 32, v34
	global_load_lds_dwordx4 v[2:3], off
	v_lshlrev_b32_e32 v2, 4, v55
	v_and_b32_e32 v37, 0x70, v2
	v_bitop3_b32 v140, v34, v35, v37 bitop3:0xde
	v_add_u32_e32 v126, 0, v140
	ds_read_b128 v[2:5], v126 offset:32768
	v_bitop3_b32 v141, v38, v35, v37 bitop3:0xde
	v_add_u32_e32 v127, 0, v141
	ds_read_b128 v[38:41], v127 offset:32768
	s_waitcnt lgkmcnt(0)
	v_mfma_f32_32x32x16_bf16 v[18:33], v[2:5], v[98:101], 0
	ds_read_b128 v[2:5], v126 offset:40960
	s_cmp_lt_i32 s38, 4
	v_mfma_f32_32x32x16_bf16 v[18:33], v[38:41], v[102:105], v[18:33]
	ds_read_b128 v[38:41], v127 offset:40960
	s_waitcnt lgkmcnt(0)
	v_mfma_f32_32x32x16_bf16 v[2:17], v[2:5], v[98:101], 0
	v_mfma_f32_32x32x16_bf16 v[2:17], v[38:41], v[102:105], v[2:17]
	v_or_b32_e32 v38, 64, v34
	v_bitop3_b32 v142, v38, v35, v37 bitop3:0xde
	v_add_u32_e32 v128, 0, v142
	ds_read_b128 v[38:41], v128 offset:32768
	s_waitcnt lgkmcnt(0)
	v_mfma_f32_32x32x16_bf16 v[18:33], v[38:41], v[106:109], v[18:33]
	ds_read_b128 v[38:41], v128 offset:40960
	s_waitcnt lgkmcnt(0)
	v_mfma_f32_32x32x16_bf16 v[2:17], v[38:41], v[106:109], v[2:17]
	v_or_b32_e32 v38, 0x60, v34
	v_bitop3_b32 v143, v38, v35, v37 bitop3:0xde
	v_add_u32_e32 v129, 0, v143
	ds_read_b128 v[38:41], v129 offset:32768
	s_waitcnt lgkmcnt(0)
	v_mfma_f32_32x32x16_bf16 v[18:33], v[38:41], v[110:113], v[18:33]
	ds_read_b128 v[38:41], v129 offset:40960
	s_waitcnt lgkmcnt(0)
	v_mfma_f32_32x32x16_bf16 v[2:17], v[38:41], v[110:113], v[2:17]
	v_or_b32_e32 v38, 0x80, v34
	v_bitop3_b32 v144, v38, v35, v37 bitop3:0xde
	v_add_u32_e32 v130, 0, v144
	ds_read_b128 v[38:41], v130 offset:32768
	v_or_b32_e32 v34, 0xa0, v34
	v_bitop3_b32 v145, v34, v35, v37 bitop3:0xde
	v_add_u32_e32 v131, 0, v145
	s_waitcnt lgkmcnt(0)
	v_mfma_f32_32x32x16_bf16 v[18:33], v[38:41], v[114:117], v[18:33]
	ds_read_b128 v[38:41], v130 offset:40960
	s_waitcnt lgkmcnt(0)
	v_mfma_f32_32x32x16_bf16 v[2:17], v[38:41], v[114:117], v[2:17]
	ds_read_b128 v[38:41], v131 offset:32768
	s_waitcnt lgkmcnt(0)
	v_mfma_f32_32x32x16_bf16 v[18:33], v[38:41], v[118:121], v[18:33]
	ds_read_b128 v[38:41], v131 offset:40960
	s_waitcnt lgkmcnt(0)
	v_mfma_f32_32x32x16_bf16 v[2:17], v[38:41], v[118:121], v[2:17]
	s_cbranch_scc1 .LBB0_1417
	s_setprio 1
; __device__ __forceinline__ void finishSM(f32x16& p0, f32x16& p1, float& l_reg, bf16x8& pa0, bf16x8& pa1, bf16x8& pa2, bf16x8& pa3) {
; #pragma unroll
;   for (int r = 0; r < 16; ++r) p1[r] = __builtin_amdgcn_exp2f(p1[r]);
;   float ps = 0;
; #pragma unroll
;   for (int r = 0; r < 16; ++r) ps += p0[r];
; #pragma unroll
;   for (int r = 0; r < 16; ++r) ps += p1[r];
;   l_reg += ps;
;     ...
;   ATT_PK4(p0, 0, pa0); ATT_PK4(p0, 8, pa1); ATT_PK4(p1, 0, pa2); ATT_PK4(p1, 8, pa3);
;     ...
; }
; template <int DK>
; __device__ __forceinline__ void qkt(f32x16& p0, f32x16& p1, const char* Ks, const bf16x8* qr, int r32, int hi) {
;   p0 = f32x16{}; p1 = f32x16{};
; #pragma unroll
;   for (int d0 = 0; d0 < DK / 16; ++d0) { const int cb = (d0 * 16 + hi * 8) * 2;
;     const bf16x8 b0 = *reinterpret_cast<const bf16x8*>(Ks + ATT_KSWZ(r32, cb));
;     const bf16x8 b1 = *reinterpret_cast<const bf16x8*>(Ks + ATT_KSWZ(32 + r32, cb));
;     p0 = __builtin_amdgcn_mfma_f32_32x32x16_bf16(b0, qr[d0], p0, 0, 0, 0);
;     p1 = __builtin_amdgcn_mfma_f32_32x32x16_bf16(b1, qr[d0], p1, 0, 0, 0);
;   }
; }
.LBB0_1417:
	s_cmp_lg_u32 0, -1
	s_cselect_b32 s1, 0, 0
	s_add_i32 s85, s81, 0xc000
	s_add_i32 s86, s81, 0xc400
	s_add_u32 s40, s20, 0x9000
	s_addc_u32 s41, s21, 0
	v_mov_b32_e32 v123, v1
	s_nop 0
	v_exp_f32_e32 v184, v18
	v_exp_f32_e32 v185, v19
	v_lshl_add_u64 v[18:19], s[40:41], 0, v[0:1]
	s_mov_b32 m0, s85
	s_add_i32 s87, s87, s0
	s_waitcnt vmcnt(3)
	s_barrier
	global_load_lds_dwordx4 v[18:19], off
	v_lshl_add_u64 v[18:19], s[40:41], 0, v[122:123]
	s_mov_b32 m0, s86
	s_mov_b64 s[40:41], 0x6000
	s_add_i32 s88, s87, 0x6000
	global_load_lds_dwordx4 v[18:19], off
	v_lshl_add_u64 v[18:19], v[124:125], 0, s[40:41]
	s_mov_b32 m0, s88
	v_exp_f32_e32 v186, v20
	global_load_lds_dwordx4 v[18:19], off
	v_exp_f32_e32 v187, v21
	v_exp_f32_e32 v188, v22
	v_exp_f32_e32 v189, v23
	v_exp_f32_e32 v190, v24
	v_exp_f32_e32 v191, v25
	ds_read_b128 v[18:21], v126 offset:49152
	ds_read_b128 v[22:25], v126 offset:57344
	v_lshlrev_b32_e32 v35, 4, v36
	v_lshlrev_b32_e32 v34, 3, v36
	v_and_b32_e32 v35, 0xc0, v35
	v_lshlrev_b32_e32 v36, 1, v36
	s_waitcnt lgkmcnt(0)
	v_mfma_f32_32x32x16_bf16 v[66:81], v[18:21], v[98:101], 0
	v_and_or_b32 v35, v34, 24, v35
	v_and_b32_e32 v36, 32, v36
	v_and_b32_e32 v34, 0x100, v34
	v_or3_b32 v148, v35, v36, v34
	v_add_u32_e32 v132, s1, v148
	v_exp_f32_e32 v192, v26
	v_exp_f32_e32 v193, v27
	v_mfma_f32_32x32x16_bf16 v[34:49], v[22:25], v[98:101], 0
	ds_read_b128 v[18:21], v127 offset:49152
	ds_read_b128 v[22:25], v127 offset:57344
	v_exp_f32_e32 v194, v28
	v_exp_f32_e32 v195, v29
	v_exp_f32_e32 v196, v30
	v_exp_f32_e32 v197, v31
	v_exp_f32_e32 v198, v32
	v_exp_f32_e32 v199, v33
	s_waitcnt lgkmcnt(0)
	v_mfma_f32_32x32x16_bf16 v[66:81], v[18:21], v[102:105], v[66:81]
	v_exp_f32_e32 v200, v2
	v_exp_f32_e32 v201, v3
	v_exp_f32_e32 v202, v4
	v_exp_f32_e32 v203, v5
	v_exp_f32_e32 v204, v6
	v_exp_f32_e32 v205, v7
	v_exp_f32_e32 v206, v8
	v_mfma_f32_32x32x16_bf16 v[34:49], v[22:25], v[102:105], v[34:49]
	ds_read_b128 v[18:21], v128 offset:49152
	ds_read_b128 v[22:25], v128 offset:57344
	v_exp_f32_e32 v207, v9
	v_exp_f32_e32 v208, v10
	v_exp_f32_e32 v209, v11
	v_exp_f32_e32 v210, v12
	v_exp_f32_e32 v211, v13
	v_exp_f32_e32 v212, v14
	s_waitcnt lgkmcnt(0)
	v_mfma_f32_32x32x16_bf16 v[66:81], v[18:21], v[106:109], v[66:81]
	v_exp_f32_e32 v213, v15
	v_exp_f32_e32 v214, v16
	v_exp_f32_e32 v215, v17
	s_and_b64 vcc, exec, s[36:37]
	v_mfma_f32_32x32x16_bf16 v[34:49], v[22:25], v[106:109], v[34:49]
	ds_read_b128 v[18:21], v129 offset:49152
	ds_read_b128 v[22:25], v129 offset:57344
	s_waitcnt lgkmcnt(0)
	v_mfma_f32_32x32x16_bf16 v[66:81], v[18:21], v[110:113], v[66:81]
	v_mfma_f32_32x32x16_bf16 v[34:49], v[22:25], v[110:113], v[34:49]
	ds_read_b128 v[18:21], v130 offset:49152
	ds_read_b128 v[22:25], v130 offset:57344
	s_waitcnt lgkmcnt(0)
	v_mfma_f32_32x32x16_bf16 v[66:81], v[18:21], v[114:117], v[66:81]
	v_mfma_f32_32x32x16_bf16 v[34:49], v[22:25], v[114:117], v[34:49]
	ds_read_b128 v[18:21], v131 offset:49152
	ds_read_b128 v[22:25], v131 offset:57344
	s_waitcnt lgkmcnt(0)
	v_mfma_f32_32x32x16_bf16 v[66:81], v[18:21], v[118:121], v[66:81]
	v_cvt_pk_bf16_f32 v18, v184, v185
	v_cvt_pk_bf16_f32 v19, v186, v187
	v_cvt_pk_bf16_f32 v20, v188, v189
	v_cvt_pk_bf16_f32 v21, v190, v191
	v_cvt_pk_bf16_f32 v50, v192, v193
	v_cvt_pk_bf16_f32 v51, v194, v195
	v_cvt_pk_bf16_f32 v52, v196, v197
	v_cvt_pk_bf16_f32 v53, v198, v199
	v_cvt_pk_bf16_f32 v54, v200, v201
	v_cvt_pk_bf16_f32 v55, v202, v203
	v_cvt_pk_bf16_f32 v56, v204, v205
	v_cvt_pk_bf16_f32 v57, v206, v207
	v_cvt_pk_bf16_f32 v58, v208, v209
	v_cvt_pk_bf16_f32 v59, v210, v211
	v_cvt_pk_bf16_f32 v60, v212, v213
	v_cvt_pk_bf16_f32 v61, v214, v215
	ds_read_b64_tr_b16 v[2:3], v132 offset:0
	ds_read_b64_tr_b16 v[4:5], v132 offset:0x400
	v_mfma_f32_32x32x16_bf16 v[34:49], v[22:25], v[118:121], v[34:49]
	ds_read_b64_tr_b16 v[22:23], v132 offset:0x800
	ds_read_b64_tr_b16 v[24:25], v132 offset:0xc00
	ds_read_b64_tr_b16 v[26:27], v132 offset:0x1000
	ds_read_b64_tr_b16 v[28:29], v132 offset:0x1400
	ds_read_b64_tr_b16 v[30:31], v132 offset:0x1800
	ds_read_b64_tr_b16 v[32:33], v132 offset:0x1c00
	ds_read_b64_tr_b16 v[62:63], v132 offset:0x200
	ds_read_b64_tr_b16 v[64:65], v132 offset:0x600
	ds_read_b64_tr_b16 v[82:83], v132 offset:0xa00
	ds_read_b64_tr_b16 v[84:85], v132 offset:0xe00
	v_permlane32_swap_b32_e32 v18, v20
	v_permlane32_swap_b32_e32 v19, v21
	ds_read_b64_tr_b16 v[86:87], v132 offset:0x1200
	ds_read_b64_tr_b16 v[88:89], v132 offset:0x1600
	ds_read_b64_tr_b16 v[90:91], v132 offset:0x1a00
	ds_read_b64_tr_b16 v[92:93], v132 offset:0x1e00
	s_waitcnt lgkmcnt(8)
	v_permlane32_swap_b32_e32 v50, v52
	s_nop 0
	v_mfma_f32_32x32x16_bf16 v[2:17], v[18:21], v[2:5], 0
	v_permlane32_swap_b32_e32 v51, v53
	v_permlane32_swap_b32_e32 v54, v56
	v_permlane32_swap_b32_e32 v55, v57
	v_permlane32_swap_b32_e32 v58, v60
	v_mfma_f32_32x32x16_bf16 v[2:17], v[50:53], v[22:25], v[2:17]
	v_permlane32_swap_b32_e32 v59, v61
	s_waitcnt lgkmcnt(0)
	s_waitcnt vmcnt(3)
	s_barrier
	v_mfma_f32_32x32x16_bf16 v[2:17], v[54:57], v[26:29], v[2:17]
	v_mfma_f32_32x32x16_bf16 v[2:17], v[58:61], v[30:33], v[2:17]
	v_mfma_f32_32x32x16_bf16 v[18:33], v[18:21], v[62:65], 0
	v_mfma_f32_32x32x16_bf16 v[18:33], v[50:53], v[82:85], v[18:33]
	v_mfma_f32_32x32x16_bf16 v[18:33], v[54:57], v[86:89], v[18:33]
	v_mfma_f32_32x32x16_bf16 v[18:33], v[58:61], v[90:93], v[18:33]
	s_cbranch_vccnz .LBB0_1419
	s_add_u32 s0, s20, 0xc000
	s_addc_u32 s1, s21, 0
	s_mov_b32 m0, s81
	v_lshl_add_u64 v[50:51], s[0:1], 0, v[0:1]
	v_lshl_add_u64 v[52:53], s[0:1], 0, v[122:123]
	s_mov_b64 s[0:1], 0x8000
	global_load_lds_dwordx4 v[50:51], off
	s_mov_b32 m0, s82
	v_lshl_add_u64 v[54:55], v[124:125], 0, s[0:1]
	global_load_lds_dwordx4 v[52:53], off
	s_mov_b32 m0, s87
	s_nop 0
	global_load_lds_dwordx4 v[54:55], off

; #define DMA_WAIT(last) do { if (last) asm volatile("s_waitcnt vmcnt(0)" ::: "memory"); else asm volatile("s_waitcnt vmcnt(%0)" :: "n"(NPW) : "memory"); } while (0)
; template <int DK, int DV, bool OFF, class QLoader> ...
;     ...
;   f32x16 pA0, pA1, pB0, pB1; bf16x8 pa0, pa1, pa2, pa3; const int NT = nkeys / KVBLK;
;   DMA_TILE(0, 0); DMA_TILE(1, 1); DMA_WAIT(false); __syncthreads(); if (2 < NT) DMA_TILE(2, 2);
;   qkt<DK>(pA0, pA1, K_lds, qr, r32, hi); partialSM<DK, OFF>(pA0, pA1, negMC);
.LBB0_1423:
	s_and_b64 vcc, exec, s[36:37]
	s_barrier
	s_cbranch_vccnz .LBB0_1425
	s_add_u32 s0, s20, 0xf000
	s_addc_u32 s1, s21, 0
	s_mov_b32 m0, s83
	v_lshl_add_u64 v[158:159], s[0:1], 0, v[0:1]
	v_lshl_add_u64 v[160:161], s[0:1], 0, v[122:123]
	s_mov_b64 s[0:1], 0xa000
	global_load_lds_dwordx4 v[158:159], off
	s_mov_b32 m0, s84
	v_lshl_add_u64 v[162:163], v[124:125], 0, s[0:1]
	global_load_lds_dwordx4 v[160:161], off
	s_add_i32 m0, s87, 0x2000
	s_nop 0
	global_load_lds_dwordx4 v[162:163], off

; __device__ __forceinline__ void finishSM(f32x16& p0, f32x16& p1, float& l_reg, bf16x8& pa0, bf16x8& pa1, bf16x8& pa2, bf16x8& pa3) {
; #pragma unroll
;   for (int r = 0; r < 16; ++r) p1[r] = __builtin_amdgcn_exp2f(p1[r]);
;   float ps = 0;
; #pragma unroll
;   for (int r = 0; r < 16; ++r) ps += p0[r];
; #pragma unroll
;   for (int r = 0; r < 16; ++r) ps += p1[r];
;   l_reg += ps;
;     ...
;   ATT_PK4(p0, 0, pa0); ATT_PK4(p0, 8, pa1); ATT_PK4(p1, 0, pa2); ATT_PK4(p1, 8, pa3);
;     ...
; }
; template <int DK>
; __device__ __forceinline__ void qkt(f32x16& p0, f32x16& p1, const char* Ks, const bf16x8* qr, int r32, int hi) {
;   p0 = f32x16{}; p1 = f32x16{};
; #pragma unroll
;   for (int d0 = 0; d0 < DK / 16; ++d0) { const int cb = (d0 * 16 + hi * 8) * 2;
;     const bf16x8 b0 = *reinterpret_cast<const bf16x8*>(Ks + ATT_KSWZ(r32, cb));
;     const bf16x8 b1 = *reinterpret_cast<const bf16x8*>(Ks + ATT_KSWZ(32 + r32, cb));
;     p0 = __builtin_amdgcn_mfma_f32_32x32x16_bf16(b0, qr[d0], p0, 0, 0, 0);
;     p1 = __builtin_amdgcn_mfma_f32_32x32x16_bf16(b1, qr[d0], p1, 0, 0, 0);
;   }
; }
.LBB0_1429:
	s_add_u32 s0, s20, 0x12000
	s_addc_u32 s1, s21, 0
	v_lshl_add_u64 v[50:51], s[0:1], 0, v[0:1]
	s_add_i32 m0, s81, 0x8000
	s_barrier
	v_lshl_add_u64 v[52:53], s[0:1], 0, v[122:123]
	s_mov_b64 s[0:1], 0xc000
	global_load_lds_dwordx4 v[50:51], off
	s_add_i32 m0, s81, 0x8400
	v_lshl_add_u64 v[54:55], v[124:125], 0, s[0:1]
	global_load_lds_dwordx4 v[52:53], off
	s_add_i32 m0, s87, 0x4000
	v_exp_f32_e32 v34, v34
	global_load_lds_dwordx4 v[54:55], off
	ds_read_b128 v[50:53], v126 offset:32768
	ds_read_b128 v[54:57], v126 offset:40960
	s_waitcnt lgkmcnt(0)
	v_mfma_f32_32x32x16_bf16 v[66:81], v[50:53], v[98:101], 0
	ds_read_b128 v[82:85], v127 offset:32768
	ds_read_b128 v[86:89], v127 offset:40960
	v_exp_f32_e32 v35, v35
	v_exp_f32_e32 v36, v36
	v_exp_f32_e32 v37, v37
	v_exp_f32_e32 v38, v38
	v_exp_f32_e32 v39, v39
	v_exp_f32_e32 v40, v40
	v_mfma_f32_32x32x16_bf16 v[50:65], v[54:57], v[98:101], 0
	v_exp_f32_e32 v41, v41
	v_exp_f32_e32 v42, v42
	v_exp_f32_e32 v43, v43
	v_exp_f32_e32 v44, v44
	v_exp_f32_e32 v45, v45
	v_exp_f32_e32 v46, v46
	v_exp_f32_e32 v47, v47
	s_waitcnt lgkmcnt(0)
	v_mfma_f32_32x32x16_bf16 v[66:81], v[82:85], v[102:105], v[66:81]
	v_exp_f32_e32 v48, v48
	v_exp_f32_e32 v49, v49
	v_add_f32_e32 v0, 0, v184
	v_add_f32_e32 v0, v186, v0
	v_add_f32_e32 v0, v185, v0
	v_add_f32_e32 v0, v187, v0
	v_add_f32_e32 v0, v189, v0
	v_mfma_f32_32x32x16_bf16 v[50:65], v[86:89], v[102:105], v[50:65]
	ds_read_b128 v[82:85], v128 offset:32768
	ds_read_b128 v[86:89], v128 offset:40960
	v_add_f32_e32 v0, v193, v0
	v_add_f32_e32 v0, v192, v0
	v_add_f32_e32 v0, v194, v0
	v_add_f32_e32 v0, v188, v0
	v_add_f32_e32 v0, v191, v0
	v_add_f32_e32 v0, v190, v0
	s_waitcnt lgkmcnt(0)
	v_mfma_f32_32x32x16_bf16 v[66:81], v[82:85], v[106:109], v[66:81]
	v_add_f32_e32 v0, v196, v0
	v_add_f32_e32 v0, v195, v0
	v_add_f32_e32 v0, v198, v0
	v_add_f32_e32 v0, v197, v0
	v_add_f32_e32 v0, v199, v0
	v_add_f32_e32 v0, v34, v0
	v_add_f32_e32 v0, v35, v0
	v_mfma_f32_32x32x16_bf16 v[50:65], v[86:89], v[106:109], v[50:65]
	ds_read_b128 v[82:85], v129 offset:32768
	ds_read_b128 v[86:89], v129 offset:40960
	v_add_f32_e32 v0, v36, v0
	v_add_f32_e32 v0, v37, v0
	v_add_f32_e32 v0, v38, v0
	v_add_f32_e32 v0, v39, v0
	v_add_f32_e32 v0, v40, v0
	v_add_f32_e32 v0, v41, v0
	s_waitcnt lgkmcnt(0)
	v_mfma_f32_32x32x16_bf16 v[66:81], v[82:85], v[110:113], v[66:81]
	v_add_f32_e32 v0, v42, v0
	v_add_f32_e32 v0, v43, v0
	v_add_f32_e32 v0, v44, v0
	v_add_f32_e32 v0, v45, v0
	v_add_f32_e32 v0, v46, v0
	v_add_f32_e32 v0, v47, v0
	v_add_f32_e32 v0, v48, v0
	v_mfma_f32_32x32x16_bf16 v[50:65], v[86:89], v[110:113], v[50:65]
	ds_read_b128 v[82:85], v130 offset:32768
	ds_read_b128 v[86:89], v130 offset:40960
	v_add_f32_e32 v0, v49, v0
	v_add_f32_e32 v145, v145, v0
	s_waitcnt lgkmcnt(0)
	v_mfma_f32_32x32x16_bf16 v[66:81], v[82:85], v[114:117], v[66:81]
	v_mfma_f32_32x32x16_bf16 v[50:65], v[86:89], v[114:117], v[50:65]
	ds_read_b128 v[82:85], v131 offset:32768
	ds_read_b128 v[86:89], v131 offset:40960
	s_waitcnt lgkmcnt(0)
	v_mfma_f32_32x32x16_bf16 v[66:81], v[82:85], v[118:121], v[66:81]
	v_mfma_f32_32x32x16_bf16 v[50:65], v[86:89], v[118:121], v[50:65]
	v_cvt_pk_bf16_f32 v86, v184, v186
	v_cvt_pk_bf16_f32 v87, v185, v187
	v_cvt_pk_bf16_f32 v88, v189, v193
	v_cvt_pk_bf16_f32 v89, v192, v194
	v_cvt_pk_bf16_f32 v82, v188, v191
	v_cvt_pk_bf16_f32 v83, v190, v196
	v_cvt_pk_bf16_f32 v84, v195, v198
	v_cvt_pk_bf16_f32 v85, v197, v199
	v_cvt_pk_bf16_f32 v90, v34, v35
	v_cvt_pk_bf16_f32 v91, v36, v37
	v_cvt_pk_bf16_f32 v92, v38, v39
	v_cvt_pk_bf16_f32 v93, v40, v41
	v_cvt_pk_bf16_f32 v122, v42, v43
	v_cvt_pk_bf16_f32 v123, v44, v45
	v_cvt_pk_bf16_f32 v124, v46, v47
	v_cvt_pk_bf16_f32 v125, v48, v49
	ds_read_b64_tr_b16 v[158:159], v96 offset:0
	ds_read_b64_tr_b16 v[160:161], v96 offset:0x400
	ds_read_b64_tr_b16 v[162:163], v96 offset:0x800
	ds_read_b64_tr_b16 v[164:165], v96 offset:0xc00
	ds_read_b64_tr_b16 v[166:167], v96 offset:0x1000
	ds_read_b64_tr_b16 v[168:169], v96 offset:0x1400
	ds_read_b64_tr_b16 v[170:171], v96 offset:0x1800
	ds_read_b64_tr_b16 v[172:173], v96 offset:0x1c00
	ds_read_b64_tr_b16 v[200:201], v96 offset:0x200
	ds_read_b64_tr_b16 v[202:203], v96 offset:0x600
	ds_read_b64_tr_b16 v[204:205], v96 offset:0xa00
	ds_read_b64_tr_b16 v[206:207], v96 offset:0xe00
	s_nop 0
	v_permlane32_swap_b32_e32 v86, v88
	v_permlane32_swap_b32_e32 v87, v89
	ds_read_b64_tr_b16 v[208:209], v96 offset:0x1200
	ds_read_b64_tr_b16 v[210:211], v96 offset:0x1600
	ds_read_b64_tr_b16 v[212:213], v96 offset:0x1a00
	ds_read_b64_tr_b16 v[214:215], v96 offset:0x1e00
	s_waitcnt lgkmcnt(8)
	v_permlane32_swap_b32_e32 v82, v84
	s_nop 0
	v_mfma_f32_32x32x16_bf16 v[2:17], v[86:89], v[158:161], v[2:17]
	s_waitcnt lgkmcnt(0)
	v_permlane32_swap_b32_e32 v83, v85
	v_permlane32_swap_b32_e32 v90, v92
	v_permlane32_swap_b32_e32 v91, v93
	v_mfma_f32_32x32x16_bf16 v[18:33], v[86:89], v[200:203], v[18:33]
	v_permlane32_swap_b32_e32 v122, v124
	v_permlane32_swap_b32_e32 v123, v125
	v_exp_f32_e32 v158, v66
	v_exp_f32_e32 v159, v67
	v_exp_f32_e32 v160, v68
	v_mfma_f32_32x32x16_bf16 v[2:17], v[82:85], v[162:165], v[2:17]
	v_exp_f32_e32 v161, v69
	v_exp_f32_e32 v162, v70
	v_exp_f32_e32 v163, v71
	v_exp_f32_e32 v174, v80
	v_exp_f32_e32 v175, v81
	v_mfma_f32_32x32x16_bf16 v[18:33], v[82:85], v[204:207], v[18:33]
	v_mfma_f32_32x32x16_bf16 v[2:17], v[90:93], v[166:169], v[2:17]
	v_exp_f32_e32 v166, v72
	v_exp_f32_e32 v167, v73
	v_exp_f32_e32 v168, v74
	v_exp_f32_e32 v169, v75
	v_mfma_f32_32x32x16_bf16 v[18:33], v[90:93], v[208:211], v[18:33]
	v_mfma_f32_32x32x16_bf16 v[2:17], v[122:125], v[170:173], v[2:17]
	v_exp_f32_e32 v170, v76
	v_exp_f32_e32 v171, v77
	v_exp_f32_e32 v172, v78
	v_exp_f32_e32 v173, v79
	v_mfma_f32_32x32x16_bf16 v[18:33], v[122:125], v[212:215], v[18:33]

; #define DMA_WAIT(last) do { if (last) asm volatile("s_waitcnt vmcnt(0)" ::: "memory"); else asm volatile("s_waitcnt vmcnt(%0)" :: "n"(NPW) : "memory"); } while (0)
; template <int DK, int DV, bool OFF, class QLoader> ...
;     ...
;   f32x16 pA0, pA1, pB0, pB1; bf16x8 pa0, pa1, pa2, pa3; const int NT = nkeys / KVBLK;
;   DMA_TILE(0, 0); DMA_TILE(1, 1); DMA_WAIT(false); __syncthreads(); if (2 < NT) DMA_TILE(2, 2);
;   qkt<DK>(pA0, pA1, K_lds, qr, r32, hi); partialSM<DK, OFF>(pA0, pA1, negMC);
.LBB0_1438:
	s_add_i32 s40, s92, 2
	s_cmp_lt_u32 s40, s89
	s_cselect_b64 s[0:1], -1, 0
	s_cmp_ge_u32 s40, s89
	s_cselect_b64 s[40:41], -1, 0
	s_and_b64 vcc, exec, s[40:41]
	s_barrier
	s_cbranch_vccnz .LBB0_1440
	v_lshl_add_u64 v[34:35], v[92:93], 0, s[12:13]
	s_mov_b64 s[94:95], 0x2a815000
	s_mov_b32 m0, s85
	v_lshl_add_u64 v[34:35], v[34:35], 0, s[94:95]
	global_load_lds_dwordx4 v[34:35], off
	v_lshl_add_u64 v[34:35], v[94:95], 0, s[12:13]
	v_lshl_add_u64 v[34:35], v[34:35], 0, s[94:95]
	s_mov_b32 m0, s86
	s_mov_b64 s[94:95], 0x30e0e000
	global_load_lds_dwordx4 v[34:35], off
	v_lshl_add_u64 v[34:35], v[90:91], 0, s[12:13]
	v_lshl_add_u64 v[34:35], v[34:35], 0, s[94:95]
	s_mov_b32 m0, s88
	s_nop 0
	global_load_lds_dwordx4 v[34:35], off

; #define DMA_WAIT(last) do { if (last) asm volatile("s_waitcnt vmcnt(0)" ::: "memory"); else asm volatile("s_waitcnt vmcnt(%0)" :: "n"(NPW) : "memory"); } while (0)
; template <int DK, int DV, bool OFF, class QLoader> ...
;     ...
;   f32x16 pA0, pA1, pB0, pB1; bf16x8 pa0, pa1, pa2, pa3; const int NT = nkeys / KVBLK;
;   DMA_TILE(0, 0); DMA_TILE(1, 1); DMA_WAIT(false); __syncthreads(); if (2 < NT) DMA_TILE(2, 2);
;   qkt<DK>(pA0, pA1, K_lds, qr, r32, hi); partialSM<DK, OFF>(pA0, pA1, negMC);
.LBB0_1445:
	s_add_i32 s38, s92, 3
	s_cmp_ge_u32 s38, s89
	s_barrier
	s_cbranch_scc1 .LBB0_1447
	v_lshl_add_u64 v[50:51], v[92:93], 0, s[12:13]
	s_mov_b64 s[38:39], 0x2a818000
	s_mov_b32 m0, s81
	v_lshl_add_u64 v[50:51], v[50:51], 0, s[38:39]
	global_load_lds_dwordx4 v[50:51], off
	v_lshl_add_u64 v[50:51], v[94:95], 0, s[12:13]
	v_lshl_add_u64 v[50:51], v[50:51], 0, s[38:39]
	s_mov_b32 m0, s82
	s_mov_b64 s[38:39], 0x30e10000
	global_load_lds_dwordx4 v[50:51], off
	v_lshl_add_u64 v[50:51], v[90:91], 0, s[12:13]
	v_lshl_add_u64 v[50:51], v[50:51], 0, s[38:39]
	s_mov_b32 m0, s87
	s_nop 0
	global_load_lds_dwordx4 v[50:51], off

; #define DMA_WAIT(last) do { if (last) asm volatile("s_waitcnt vmcnt(0)" ::: "memory"); else asm volatile("s_waitcnt vmcnt(%0)" :: "n"(NPW) : "memory"); } while (0)
; template <int DK, int DV, bool OFF, class QLoader> ...
;     ...
;   f32x16 pA0, pA1, pB0, pB1; bf16x8 pa0, pa1, pa2, pa3; const int NT = nkeys / KVBLK;
;   DMA_TILE(0, 0); DMA_TILE(1, 1); DMA_WAIT(false); __syncthreads(); if (2 < NT) DMA_TILE(2, 2);
;   qkt<DK>(pA0, pA1, K_lds, qr, r32, hi); partialSM<DK, OFF>(pA0, pA1, negMC);
.LBB0_1454:
	s_add_i32 s0, s92, 4
	s_cmp_ge_u32 s0, s89
	s_barrier
	s_cbranch_scc1 .LBB0_1456
	v_lshl_add_u64 v[34:35], v[92:93], 0, s[12:13]
	s_mov_b64 s[0:1], 0x2a81b000
	s_mov_b32 m0, s83
	v_lshl_add_u64 v[34:35], v[34:35], 0, s[0:1]
	global_load_lds_dwordx4 v[34:35], off
	v_lshl_add_u64 v[34:35], v[94:95], 0, s[12:13]
	v_lshl_add_u64 v[34:35], v[34:35], 0, s[0:1]
	s_mov_b32 m0, s84
	s_mov_b64 s[0:1], 0x30e12000
	global_load_lds_dwordx4 v[34:35], off
	v_lshl_add_u64 v[34:35], v[90:91], 0, s[12:13]
	v_lshl_add_u64 v[34:35], v[34:35], 0, s[0:1]
	s_add_i32 m0, s87, 0x2000
	s_nop 0
	global_load_lds_dwordx4 v[34:35], off

; #define DMA_WAIT(last) do { if (last) asm volatile("s_waitcnt vmcnt(0)" ::: "memory"); else asm volatile("s_waitcnt vmcnt(%0)" :: "n"(NPW) : "memory"); } while (0)
; template <int DK, int DV, bool OFF, class QLoader> ...
;     ...
;   f32x16 pA0, pA1, pB0, pB1; bf16x8 pa0, pa1, pa2, pa3; const int NT = nkeys / KVBLK;
;   DMA_TILE(0, 0); DMA_TILE(1, 1); DMA_WAIT(false); __syncthreads(); if (2 < NT) DMA_TILE(2, 2);
;   qkt<DK>(pA0, pA1, K_lds, qr, r32, hi); partialSM<DK, OFF>(pA0, pA1, negMC);
.LBB0_1461:
	s_add_i32 s0, s92, 5
	s_cmp_ge_u32 s0, s89
	s_barrier
	s_cbranch_scc1 .LBB0_1432
	v_lshl_add_u64 v[50:51], v[92:93], 0, s[12:13]
	s_mov_b64 s[0:1], 0x2a81e000
	v_lshl_add_u64 v[50:51], v[50:51], 0, s[0:1]
	s_add_i32 m0, s81, 0x8000
	s_nop 0
	global_load_lds_dwordx4 v[50:51], off
	v_lshl_add_u64 v[50:51], v[94:95], 0, s[12:13]
	v_lshl_add_u64 v[50:51], v[50:51], 0, s[0:1]
	s_add_i32 m0, s81, 0x8400
	s_mov_b64 s[0:1], 0x30e14000
	global_load_lds_dwordx4 v[50:51], off
	v_lshl_add_u64 v[50:51], v[90:91], 0, s[12:13]
	v_lshl_add_u64 v[50:51], v[50:51], 0, s[0:1]
	s_add_i32 m0, s87, 0x4000
	s_nop 0
	global_load_lds_dwordx4 v[50:51], off
	s_branch .LBB0_1432
